# split grid barrier 2 for non-scan blocks: conversion and meta ml_out blocks arrive at the seam and wait before their barrier-3 arrive
# speedup vs baseline: 1.0175x; 1.0081x over previous
.Lgb_chk_2:
	v_mov_b32_e32 v11, s89
	v_cmp_gt_u32_e32 vcc, 0x88, v11
	s_cbranch_vccz .Lgb_done_2

.LBB0_601:
	s_andn2_b64 vcc, exec, s[10:11]
	s_mov_b32 s46, s9
	s_cbranch_vccnz .LBB0_655
	s_waitcnt vmcnt(0)
	s_barrier
	s_mov_b64 s[10:11], exec
	v_readlane_b32 s44, v254, 12
	v_readlane_b32 s45, v254, 13
	s_and_b64 s[44:45], s[10:11], s[44:45]
	s_mov_b64 exec, s[44:45]
	s_cbranch_execz .LBB0_654
	v_mov_b32_e32 v7, v254
	v_cmp_gt_u32_e32 vcc, 0x88, v7
	s_cbranch_vccnz .Lgw_end_2
	v_mov_b32_e32 v8, 0x22160
	ds_read_b32 v9, v8
	v_mov_b32_e32 v10, s99
	v_lshrrev_b32_e32 v11, 16, v10
	v_mov_b32_e32 v12, s98
	v_min_u32_e32 v12, 8, v12
	v_mov_b32_e32 v13, 0
	s_waitcnt lgkmcnt(0)
	v_mul_lo_u32 v12, v12, v9

.Lgw_end_2:
	v_mov_b32_e32 v7, 0x22160
	s_waitcnt vmcnt(0) lgkmcnt(0)
	ds_read_b32 v8, v7
	v_mov_b32_e32 v9, 1
	v_mov_b32_e32 v10, s99
	v_and_b32_e32 v11, 0xffff, v10
	v_lshrrev_b32_e32 v12, 16, v10
	global_atomic_add v13, v11, v9, s[100:101] sc0
	buffer_inv sc1
	v_lshrrev_b32_e32 v14, 8, v11
	v_sub_u32_e32 v14, s98, v14
	v_add_u32_e32 v14, 7, v14
	v_lshrrev_b32_e32 v14, 3, v14
	v_mov_b32_e32 v15, s98
	v_min_u32_e32 v15, 8, v15
	v_mov_b32_e32 v16, 0
	s_waitcnt lgkmcnt(0)
	v_add_u32_e32 v8, 1, v8
	ds_write_b32 v7, v8
	v_mul_lo_u32 v14, v14, v8
	v_mul_lo_u32 v15, v15, v8
	s_waitcnt vmcnt(0)
	v_add_u32_e32 v13, 1, v13
	v_cmp_eq_u32_e32 vcc, v13, v14
	s_cbranch_vccz .Lgb_done_3
	v_mov_b32_e32 v10, 0
	global_atomic_add v10, v9, s[100:101] offset:2048
	global_atomic_add v10, v9, s[100:101] offset:2304
	global_atomic_add v10, v9, s[100:101] offset:2560
	global_atomic_add v10, v9, s[100:101] offset:2816
	global_atomic_add v10, v9, s[100:101] offset:3072
	global_atomic_add v10, v9, s[100:101] offset:3328
	global_atomic_add v10, v9, s[100:101] offset:3584
	global_atomic_add v10, v9, s[100:101] offset:3840
